# layers 1-3: first node's edge-row loads issued right after the rowptr barrier (overlap the source-index staging); self rows added at pass end; no entry self-row load
# baseline (speedup 1.0000x reference)
_Z12layer_kernelILb0ELi256ELi32EEvPKDv8_DF16_PKfPS0_PiS6_S6_S2_S4_S5_PfPK15HIP_vector_typeIiLj2EEPKi:
	s_load_dword s3, s[0:1], 0x60
	s_load_dwordx2 s[26:27], s[0:1], 0x38
	s_load_dwordx2 s[28:29], s[0:1], 0x0
	s_load_dwordx2 s[14:15], s[0:1], 0x20
	s_load_dwordx2 s[8:9], s[0:1], 0x18
	s_load_dwordx2 s[30:31], s[0:1], 0x10
	s_waitcnt lgkmcnt(0)
	s_load_dword s16, s[26:27], 0x0
	s_ashr_i32 s4, s3, 3
	s_and_b32 s5, s3, 7
	s_and_b32 s3, s2, 7
	s_add_i32 s10, s4, 1
	s_cmp_ge_u32 s3, s5
	s_cbranch_scc0 .LBB5_2
	s_mul_i32 s6, s10, s5
	s_sub_i32 s5, s3, s5
	s_mul_i32 s5, s5, s4
	s_add_i32 s11, s6, s5
	s_cbranch_execz .LBB5_3
	s_branch .LBB5_4

.Llay_fwd:
	v_lshrrev_b32_e32 v35, 3, v0
	s_lshl_b32 s24, s25, 5
	v_and_b32_e32 v60, 30, v35
	v_or_b32_e32 v8, s24, v60
	v_min_i32_e32 v2, 0x1869f, v8
	v_ashrrev_i32_e32 v3, 31, v2
	v_and_b32_e32 v1, 15, v0
	v_lshlrev_b64 v[2:3], 8, v[2:3]
	v_mov_b32_e32 v27, 0
	v_lshl_add_u64 v[2:3], s[4:5], 0, v[2:3]
	v_lshlrev_b32_e32 v26, 4, v1
	v_lshl_add_u64 v[2:3], v[2:3], 0, v[26:27]
	s_mov_b32 s28, 0
	v_cmp_gt_u32_e32 vcc, 33, v0
	s_and_saveexec_b64 s[2:3], vcc
	s_cbranch_execz .LBB5_6
	v_add_u32_e32 v6, s24, v0
	v_min_i32_e32 v6, 0x186a0, v6
	v_ashrrev_i32_e32 v7, 31, v6
	v_lshl_add_u64 v[6:7], v[6:7], 2, s[8:9]
	global_load_dword v6, v[6:7], off
	v_lshlrev_b32_e32 v7, 2, v0
	s_waitcnt vmcnt(0)
	ds_write_b32 v7, v6 offset:12800
.LBB5_6:
	s_or_b64 exec, exec, s[2:3]
	s_movk_i32 s2, 0x3000
	v_add_u32_e64 v6, s2, 0
	s_waitcnt lgkmcnt(0)
	s_barrier
	ds_read2_b32 v[28:29], v6 offset0:128 offset1:160
	s_load_dwordx2 s[8:9], s[0:1], 0x48
	s_load_dwordx2 s[10:11], s[0:1], 0x30
	s_waitcnt lgkmcnt(0)
	v_sub_u32_e32 v6, v29, v28
	v_cmp_gt_i32_e32 vcc, 0x401, v6
	s_cbranch_vccz .Ll1e_noearly
	s_mov_b32 s28, 1
	v_add_f32_e64 v34, s16, 1.0
	v_lshlrev_b32_e32 v46, 2, v60
	ds_read_b64 v[44:45], v46 offset:12800
	s_waitcnt lgkmcnt(0)
	v_lshl_add_u32 v29, v44, 8, v26
	v_cmp_lt_i32_e64 s[16:17], v44, v45
	v_add_u32_e32 v46, 1, v44
	v_cmp_lt_i32_e64 s[18:19], v46, v45
	v_add_u32_e32 v46, 2, v44
	v_cmp_lt_i32_e64 s[20:21], v46, v45
	v_add_u32_e32 v46, 3, v44
	v_cmp_lt_i32_e64 s[22:23], v46, v45
	s_mov_b64 s[2:3], exec
	s_mov_b64 exec, s[16:17]
	global_load_dwordx4 v[2:5], v29, s[30:31] offset:0
	s_mov_b64 exec, s[18:19]
	global_load_dwordx4 v[14:17], v29, s[30:31] offset:256
	s_mov_b64 exec, s[20:21]
	global_load_dwordx4 v[22:25], v29, s[30:31] offset:512
	s_mov_b64 exec, s[22:23]
	global_load_dwordx4 v[54:57], v29, s[30:31] offset:768
	s_mov_b64 exec, s[2:3]
.Ll1e_noearly:
	v_cmp_gt_i32_e32 vcc, v6, v0
	s_and_saveexec_b64 s[2:3], vcc
	s_cbranch_execz .LBB5_9
	v_min_i32_e32 v9, 0x400, v6
	v_add_u32_e32 v6, v0, v28
	v_ashrrev_i32_e32 v7, 31, v6
	v_mov_b32_e32 v10, 0x2200
	v_lshl_add_u64 v[6:7], v[6:7], 2, s[14:15]
	v_lshl_add_u32 v10, v0, 2, v10
	s_mov_b64 s[6:7], 0
	s_mov_b64 s[12:13], 0x400
	v_mov_b32_e32 v11, v0

.LBB5_9:
	s_or_b64 exec, exec, s[2:3]
	v_mov_b32_e32 v27, 0
	s_load_dwordx2 s[6:7], s[0:1], 0x40
	s_load_dwordx2 s[12:13], s[0:1], 0x10
	s_waitcnt lgkmcnt(0)
	s_barrier
	s_cmp_eq_u32 s28, 1
	s_cbranch_scc1 .Ll1e_fits
	global_load_dwordx4 v[2:5], v[2:3], off
	v_lshlrev_b32_e32 v7, 2, v60
	ds_read_b32 v6, v27 offset:12928
	ds_read_b64 v[44:45], v7 offset:12800
	s_mov_b32 s0, 0x186a0
	v_add_f32_e64 v34, s16, 1.0
	v_cmp_gt_i32_e32 vcc, s0, v8
	v_mov_b32_e32 v42, 0
	v_mov_b32_e32 v43, 0
	v_mov_b32_e32 v40, 0
	v_mov_b32_e32 v41, 0
	v_mov_b32_e32 v38, 0
	v_mov_b32_e32 v39, 0
	v_mov_b32_e32 v36, 0
	v_mov_b32_e32 v37, 0
	s_and_saveexec_b64 s[0:1], vcc
	s_cbranch_execz .LBB5_11
	s_waitcnt vmcnt(0)
	v_cvt_f32_f16_sdwa v9, v2 dst_sel:DWORD dst_unused:UNUSED_PAD src0_sel:WORD_1
	v_cvt_f32_f16_sdwa v11, v3 dst_sel:DWORD dst_unused:UNUSED_PAD src0_sel:WORD_1
	v_cvt_f32_f16_sdwa v13, v4 dst_sel:DWORD dst_unused:UNUSED_PAD src0_sel:WORD_1
	v_cvt_f32_f16_sdwa v15, v5 dst_sel:DWORD dst_unused:UNUSED_PAD src0_sel:WORD_1
	v_cvt_f32_f16_e32 v14, v5
	v_cvt_f32_f16_e32 v12, v4
	v_cvt_f32_f16_e32 v10, v3
	v_cvt_f32_f16_e32 v8, v2
	v_pk_mul_f32 v[36:37], v[34:35], v[14:15] op_sel_hi:[0,1]
	v_pk_mul_f32 v[38:39], v[34:35], v[12:13] op_sel_hi:[0,1]
	v_pk_mul_f32 v[40:41], v[34:35], v[10:11] op_sel_hi:[0,1]
	v_pk_mul_f32 v[42:43], v[34:35], v[8:9] op_sel_hi:[0,1]

.LBB5_24:
.Ll1e_fits:
	s_mov_b64 s[2:3], exec
	s_movk_i32 s1, 0x2200
	v_add_u32_e32 v47, s24, v60
	s_mov_b32 s0, 0x186a0
	v_cmp_gt_i32_e32 vcc, s0, v47
	s_mov_b64 s[14:15], vcc
	v_min_i32_e32 v47, 0x1869f, v47
	v_lshl_add_u32 v47, v47, 8, v26
	global_load_dwordx4 v[30:33], v47, s[4:5]
	v_mov_b32_e32 v36, 0
	v_mov_b32_e32 v37, 0
	v_mov_b32_e32 v38, 0
	v_mov_b32_e32 v39, 0
	v_mov_b32_e32 v40, 0
	v_mov_b32_e32 v41, 0
	v_mov_b32_e32 v42, 0
	v_mov_b32_e32 v43, 0
	v_sub_u32_e32 v27, v44, v28
	v_lshl_add_u32 v27, v27, 2, s1
	s_mov_b64 exec, s[16:17]
	ds_read_b32 v10, v27 offset:0
	s_mov_b64 exec, s[18:19]
	ds_read_b32 v11, v27 offset:4
	s_mov_b64 exec, s[20:21]
	ds_read_b32 v12, v27 offset:8
	s_mov_b64 exec, s[22:23]
	ds_read_b32 v13, v27 offset:12
	s_mov_b64 exec, s[16:17]
	s_waitcnt lgkmcnt(0)
	v_lshl_add_u32 v10, v10, 8, v26
	global_load_dwordx4 v[6:9], v10, s[4:5]
	ds_read_b32 v10, v27 offset:16
	s_mov_b64 exec, s[18:19]
	s_waitcnt lgkmcnt(0)
	v_lshl_add_u32 v11, v11, 8, v26
	global_load_dwordx4 v[18:21], v11, s[4:5]
	ds_read_b32 v11, v27 offset:20
	s_mov_b64 exec, s[20:21]
	s_waitcnt lgkmcnt(0)
	v_lshl_add_u32 v12, v12, 8, v26
	global_load_dwordx4 v[50:53], v12, s[4:5]
	ds_read_b32 v12, v27 offset:24
	s_mov_b64 exec, s[22:23]
	s_waitcnt lgkmcnt(0)
	v_lshl_add_u32 v13, v13, 8, v26
	global_load_dwordx4 v[58:61], v13, s[4:5]
	ds_read_b32 v13, v27 offset:28
	s_mov_b64 exec, s[2:3]
	s_cmp_eq_u64 s[16:17], 0
	s_cbranch_scc1 .Ll1e_p1_empty
	s_mov_b64 exec, s[16:17]
	s_waitcnt vmcnt(3)
	v_fma_mix_f32 v46, v6, 1.0, v2 op_sel_hi:[1,0,1]
	v_fma_mix_f32 v47, v6, 1.0, v2 op_sel:[1,0,1] op_sel_hi:[1,0,1]
	v_fma_mix_f32 v48, v7, 1.0, v3 op_sel_hi:[1,0,1]
	v_fma_mix_f32 v49, v7, 1.0, v3 op_sel:[1,0,1] op_sel_hi:[1,0,1]
	v_max_f32_e32 v46, 0, v46
	v_max_f32_e32 v47, 0, v47
	v_max_f32_e32 v48, 0, v48
	v_max_f32_e32 v49, 0, v49
	v_pk_add_f32 v[42:43], v[42:43], v[46:47]
	v_pk_add_f32 v[40:41], v[40:41], v[48:49]
	v_fma_mix_f32 v46, v8, 1.0, v4 op_sel_hi:[1,0,1]
	v_fma_mix_f32 v47, v8, 1.0, v4 op_sel:[1,0,1] op_sel_hi:[1,0,1]
	v_fma_mix_f32 v48, v9, 1.0, v5 op_sel_hi:[1,0,1]
	v_fma_mix_f32 v49, v9, 1.0, v5 op_sel:[1,0,1] op_sel_hi:[1,0,1]
	v_max_f32_e32 v46, 0, v46
	v_max_f32_e32 v47, 0, v47
	v_max_f32_e32 v48, 0, v48
	v_max_f32_e32 v49, 0, v49
	v_pk_add_f32 v[38:39], v[38:39], v[46:47]
	v_pk_add_f32 v[36:37], v[36:37], v[48:49]
	v_add_u32_e32 v46, 4, v44
	v_cmp_lt_i32_e64 s[16:17], v46, v45
	s_mov_b64 exec, s[16:17]
	global_load_dwordx4 v[2:5], v29, s[30:31] offset:1024
	s_waitcnt lgkmcnt(0)
	v_lshl_add_u32 v10, v10, 8, v26
	global_load_dwordx4 v[6:9], v10, s[4:5]
	ds_read_b32 v10, v27 offset:32
	s_mov_b64 exec, s[18:19]
	s_waitcnt vmcnt(4)
	v_fma_mix_f32 v46, v18, 1.0, v14 op_sel_hi:[1,0,1]
	v_fma_mix_f32 v47, v18, 1.0, v14 op_sel:[1,0,1] op_sel_hi:[1,0,1]
	v_fma_mix_f32 v48, v19, 1.0, v15 op_sel_hi:[1,0,1]
	v_fma_mix_f32 v49, v19, 1.0, v15 op_sel:[1,0,1] op_sel_hi:[1,0,1]
	v_max_f32_e32 v46, 0, v46
	v_max_f32_e32 v47, 0, v47
	v_max_f32_e32 v48, 0, v48
	v_max_f32_e32 v49, 0, v49
	v_pk_add_f32 v[42:43], v[42:43], v[46:47]
	v_pk_add_f32 v[40:41], v[40:41], v[48:49]
	v_fma_mix_f32 v46, v20, 1.0, v16 op_sel_hi:[1,0,1]
	v_fma_mix_f32 v47, v20, 1.0, v16 op_sel:[1,0,1] op_sel_hi:[1,0,1]
	v_fma_mix_f32 v48, v21, 1.0, v17 op_sel_hi:[1,0,1]
	v_fma_mix_f32 v49, v21, 1.0, v17 op_sel:[1,0,1] op_sel_hi:[1,0,1]
	v_max_f32_e32 v46, 0, v46
	v_max_f32_e32 v47, 0, v47
	v_max_f32_e32 v48, 0, v48
	v_max_f32_e32 v49, 0, v49
	v_pk_add_f32 v[38:39], v[38:39], v[46:47]
	v_pk_add_f32 v[36:37], v[36:37], v[48:49]
	v_add_u32_e32 v46, 5, v44
	v_cmp_lt_i32_e64 s[18:19], v46, v45
	s_mov_b64 exec, s[18:19]
	global_load_dwordx4 v[14:17], v29, s[30:31] offset:1280
	s_waitcnt lgkmcnt(0)
	v_lshl_add_u32 v11, v11, 8, v26
	global_load_dwordx4 v[18:21], v11, s[4:5]
	ds_read_b32 v11, v27 offset:36
	s_mov_b64 exec, s[20:21]
	s_waitcnt vmcnt(5)
	v_fma_mix_f32 v46, v50, 1.0, v22 op_sel_hi:[1,0,1]
	v_fma_mix_f32 v47, v50, 1.0, v22 op_sel:[1,0,1] op_sel_hi:[1,0,1]
	v_fma_mix_f32 v48, v51, 1.0, v23 op_sel_hi:[1,0,1]
	v_fma_mix_f32 v49, v51, 1.0, v23 op_sel:[1,0,1] op_sel_hi:[1,0,1]
	v_max_f32_e32 v46, 0, v46
	v_max_f32_e32 v47, 0, v47
	v_max_f32_e32 v48, 0, v48
	v_max_f32_e32 v49, 0, v49
	v_pk_add_f32 v[42:43], v[42:43], v[46:47]
	v_pk_add_f32 v[40:41], v[40:41], v[48:49]
	v_fma_mix_f32 v46, v52, 1.0, v24 op_sel_hi:[1,0,1]
	v_fma_mix_f32 v47, v52, 1.0, v24 op_sel:[1,0,1] op_sel_hi:[1,0,1]
	v_fma_mix_f32 v48, v53, 1.0, v25 op_sel_hi:[1,0,1]
	v_fma_mix_f32 v49, v53, 1.0, v25 op_sel:[1,0,1] op_sel_hi:[1,0,1]
	v_max_f32_e32 v46, 0, v46
	v_max_f32_e32 v47, 0, v47
	v_max_f32_e32 v48, 0, v48
	v_max_f32_e32 v49, 0, v49
	v_pk_add_f32 v[38:39], v[38:39], v[46:47]
	v_pk_add_f32 v[36:37], v[36:37], v[48:49]
	v_add_u32_e32 v46, 6, v44
	v_cmp_lt_i32_e64 s[20:21], v46, v45
	s_mov_b64 exec, s[20:21]
	global_load_dwordx4 v[22:25], v29, s[30:31] offset:1536
	s_waitcnt lgkmcnt(0)
	v_lshl_add_u32 v12, v12, 8, v26
	global_load_dwordx4 v[50:53], v12, s[4:5]
	ds_read_b32 v12, v27 offset:40
	s_mov_b64 exec, s[22:23]
	s_waitcnt vmcnt(6)
	v_fma_mix_f32 v46, v58, 1.0, v54 op_sel_hi:[1,0,1]
	v_fma_mix_f32 v47, v58, 1.0, v54 op_sel:[1,0,1] op_sel_hi:[1,0,1]
	v_fma_mix_f32 v48, v59, 1.0, v55 op_sel_hi:[1,0,1]
	v_fma_mix_f32 v49, v59, 1.0, v55 op_sel:[1,0,1] op_sel_hi:[1,0,1]
	v_max_f32_e32 v46, 0, v46
	v_max_f32_e32 v47, 0, v47
	v_max_f32_e32 v48, 0, v48
	v_max_f32_e32 v49, 0, v49
	v_pk_add_f32 v[42:43], v[42:43], v[46:47]
	v_pk_add_f32 v[40:41], v[40:41], v[48:49]
	v_fma_mix_f32 v46, v60, 1.0, v56 op_sel_hi:[1,0,1]
	v_fma_mix_f32 v47, v60, 1.0, v56 op_sel:[1,0,1] op_sel_hi:[1,0,1]
	v_fma_mix_f32 v48, v61, 1.0, v57 op_sel_hi:[1,0,1]
	v_fma_mix_f32 v49, v61, 1.0, v57 op_sel:[1,0,1] op_sel_hi:[1,0,1]
	v_max_f32_e32 v46, 0, v46
	v_max_f32_e32 v47, 0, v47
	v_max_f32_e32 v48, 0, v48
	v_max_f32_e32 v49, 0, v49
	v_pk_add_f32 v[38:39], v[38:39], v[46:47]
	v_pk_add_f32 v[36:37], v[36:37], v[48:49]
	v_add_u32_e32 v46, 7, v44
	v_cmp_lt_i32_e64 s[22:23], v46, v45
	s_mov_b64 exec, s[22:23]
	global_load_dwordx4 v[54:57], v29, s[30:31] offset:1792
	s_waitcnt lgkmcnt(0)
	v_lshl_add_u32 v13, v13, 8, v26
	global_load_dwordx4 v[58:61], v13, s[4:5]
	ds_read_b32 v13, v27 offset:44
	s_mov_b64 exec, s[2:3]
	v_add_u32_e32 v44, 4, v44
	v_add_u32_e32 v27, 16, v27
	v_add_u32_e32 v29, 0x400, v29
	s_cmp_lg_u64 s[16:17], 0
	s_cbranch_scc0 .Ll1e_p1_done
.Ll1e_p1_loop:
	s_mov_b64 exec, s[16:17]
	s_waitcnt vmcnt(6)
	v_fma_mix_f32 v46, v6, 1.0, v2 op_sel_hi:[1,0,1]
	v_fma_mix_f32 v47, v6, 1.0, v2 op_sel:[1,0,1] op_sel_hi:[1,0,1]
	v_fma_mix_f32 v48, v7, 1.0, v3 op_sel_hi:[1,0,1]
	v_fma_mix_f32 v49, v7, 1.0, v3 op_sel:[1,0,1] op_sel_hi:[1,0,1]
	v_max_f32_e32 v46, 0, v46
	v_max_f32_e32 v47, 0, v47
	v_max_f32_e32 v48, 0, v48
	v_max_f32_e32 v49, 0, v49
	v_pk_add_f32 v[42:43], v[42:43], v[46:47]
	v_pk_add_f32 v[40:41], v[40:41], v[48:49]
	v_fma_mix_f32 v46, v8, 1.0, v4 op_sel_hi:[1,0,1]
	v_fma_mix_f32 v47, v8, 1.0, v4 op_sel:[1,0,1] op_sel_hi:[1,0,1]
	v_fma_mix_f32 v48, v9, 1.0, v5 op_sel_hi:[1,0,1]
	v_fma_mix_f32 v49, v9, 1.0, v5 op_sel:[1,0,1] op_sel_hi:[1,0,1]
	v_max_f32_e32 v46, 0, v46
	v_max_f32_e32 v47, 0, v47
	v_max_f32_e32 v48, 0, v48
	v_max_f32_e32 v49, 0, v49
	v_pk_add_f32 v[38:39], v[38:39], v[46:47]
	v_pk_add_f32 v[36:37], v[36:37], v[48:49]
	v_add_u32_e32 v46, 4, v44
	v_cmp_lt_i32_e64 s[16:17], v46, v45
	s_mov_b64 exec, s[16:17]
	global_load_dwordx4 v[2:5], v29, s[30:31] offset:1024
	s_waitcnt lgkmcnt(0)
	v_lshl_add_u32 v10, v10, 8, v26
	global_load_dwordx4 v[6:9], v10, s[4:5]
	ds_read_b32 v10, v27 offset:32
	s_mov_b64 exec, s[18:19]
	s_waitcnt vmcnt(6)
	v_fma_mix_f32 v46, v18, 1.0, v14 op_sel_hi:[1,0,1]
	v_fma_mix_f32 v47, v18, 1.0, v14 op_sel:[1,0,1] op_sel_hi:[1,0,1]
	v_fma_mix_f32 v48, v19, 1.0, v15 op_sel_hi:[1,0,1]
	v_fma_mix_f32 v49, v19, 1.0, v15 op_sel:[1,0,1] op_sel_hi:[1,0,1]
	v_max_f32_e32 v46, 0, v46
	v_max_f32_e32 v47, 0, v47
	v_max_f32_e32 v48, 0, v48
	v_max_f32_e32 v49, 0, v49
	v_pk_add_f32 v[42:43], v[42:43], v[46:47]
	v_pk_add_f32 v[40:41], v[40:41], v[48:49]
	v_fma_mix_f32 v46, v20, 1.0, v16 op_sel_hi:[1,0,1]
	v_fma_mix_f32 v47, v20, 1.0, v16 op_sel:[1,0,1] op_sel_hi:[1,0,1]
	v_fma_mix_f32 v48, v21, 1.0, v17 op_sel_hi:[1,0,1]
	v_fma_mix_f32 v49, v21, 1.0, v17 op_sel:[1,0,1] op_sel_hi:[1,0,1]
	v_max_f32_e32 v46, 0, v46
	v_max_f32_e32 v47, 0, v47
	v_max_f32_e32 v48, 0, v48
	v_max_f32_e32 v49, 0, v49
	v_pk_add_f32 v[38:39], v[38:39], v[46:47]
	v_pk_add_f32 v[36:37], v[36:37], v[48:49]
	v_add_u32_e32 v46, 5, v44
	v_cmp_lt_i32_e64 s[18:19], v46, v45
	s_mov_b64 exec, s[18:19]
	global_load_dwordx4 v[14:17], v29, s[30:31] offset:1280
	s_waitcnt lgkmcnt(0)
	v_lshl_add_u32 v11, v11, 8, v26
	global_load_dwordx4 v[18:21], v11, s[4:5]
	ds_read_b32 v11, v27 offset:36
	s_mov_b64 exec, s[20:21]
	s_waitcnt vmcnt(6)
	v_fma_mix_f32 v46, v50, 1.0, v22 op_sel_hi:[1,0,1]
	v_fma_mix_f32 v47, v50, 1.0, v22 op_sel:[1,0,1] op_sel_hi:[1,0,1]
	v_fma_mix_f32 v48, v51, 1.0, v23 op_sel_hi:[1,0,1]
	v_fma_mix_f32 v49, v51, 1.0, v23 op_sel:[1,0,1] op_sel_hi:[1,0,1]
	v_max_f32_e32 v46, 0, v46
	v_max_f32_e32 v47, 0, v47
	v_max_f32_e32 v48, 0, v48
	v_max_f32_e32 v49, 0, v49
	v_pk_add_f32 v[42:43], v[42:43], v[46:47]
	v_pk_add_f32 v[40:41], v[40:41], v[48:49]
	v_fma_mix_f32 v46, v52, 1.0, v24 op_sel_hi:[1,0,1]
	v_fma_mix_f32 v47, v52, 1.0, v24 op_sel:[1,0,1] op_sel_hi:[1,0,1]
	v_fma_mix_f32 v48, v53, 1.0, v25 op_sel_hi:[1,0,1]
	v_fma_mix_f32 v49, v53, 1.0, v25 op_sel:[1,0,1] op_sel_hi:[1,0,1]
	v_max_f32_e32 v46, 0, v46
	v_max_f32_e32 v47, 0, v47
	v_max_f32_e32 v48, 0, v48
	v_max_f32_e32 v49, 0, v49
	v_pk_add_f32 v[38:39], v[38:39], v[46:47]
	v_pk_add_f32 v[36:37], v[36:37], v[48:49]
	v_add_u32_e32 v46, 6, v44
	v_cmp_lt_i32_e64 s[20:21], v46, v45
	s_mov_b64 exec, s[20:21]
	global_load_dwordx4 v[22:25], v29, s[30:31] offset:1536
	s_waitcnt lgkmcnt(0)
	v_lshl_add_u32 v12, v12, 8, v26
	global_load_dwordx4 v[50:53], v12, s[4:5]
	ds_read_b32 v12, v27 offset:40
	s_mov_b64 exec, s[22:23]
	s_waitcnt vmcnt(6)
	v_fma_mix_f32 v46, v58, 1.0, v54 op_sel_hi:[1,0,1]
	v_fma_mix_f32 v47, v58, 1.0, v54 op_sel:[1,0,1] op_sel_hi:[1,0,1]
	v_fma_mix_f32 v48, v59, 1.0, v55 op_sel_hi:[1,0,1]
	v_fma_mix_f32 v49, v59, 1.0, v55 op_sel:[1,0,1] op_sel_hi:[1,0,1]
	v_max_f32_e32 v46, 0, v46
	v_max_f32_e32 v47, 0, v47
	v_max_f32_e32 v48, 0, v48
	v_max_f32_e32 v49, 0, v49
	v_pk_add_f32 v[42:43], v[42:43], v[46:47]
	v_pk_add_f32 v[40:41], v[40:41], v[48:49]
	v_fma_mix_f32 v46, v60, 1.0, v56 op_sel_hi:[1,0,1]
	v_fma_mix_f32 v47, v60, 1.0, v56 op_sel:[1,0,1] op_sel_hi:[1,0,1]
	v_fma_mix_f32 v48, v61, 1.0, v57 op_sel_hi:[1,0,1]
	v_fma_mix_f32 v49, v61, 1.0, v57 op_sel:[1,0,1] op_sel_hi:[1,0,1]
	v_max_f32_e32 v46, 0, v46
	v_max_f32_e32 v47, 0, v47
	v_max_f32_e32 v48, 0, v48
	v_max_f32_e32 v49, 0, v49
	v_pk_add_f32 v[38:39], v[38:39], v[46:47]
	v_pk_add_f32 v[36:37], v[36:37], v[48:49]
	v_add_u32_e32 v46, 7, v44
	v_cmp_lt_i32_e64 s[22:23], v46, v45
	s_mov_b64 exec, s[22:23]
	global_load_dwordx4 v[54:57], v29, s[30:31] offset:1792
	s_waitcnt lgkmcnt(0)
	v_lshl_add_u32 v13, v13, 8, v26
	global_load_dwordx4 v[58:61], v13, s[4:5]
	ds_read_b32 v13, v27 offset:44
	s_mov_b64 exec, s[2:3]
	v_add_u32_e32 v44, 4, v44
	v_add_u32_e32 v27, 16, v27
	v_add_u32_e32 v29, 0x400, v29
	s_cmp_lg_u64 s[16:17], 0
	s_cbranch_scc1 .Ll1e_p1_loop
	s_branch .Ll1e_p1_done

.Ll1e_p1_done:
	v_cvt_f32_f16_e32 v2, v30
	v_cvt_f32_f16_sdwa v3, v30 dst_sel:DWORD dst_unused:UNUSED_PAD src0_sel:WORD_1
	v_cvt_f32_f16_e32 v4, v31
	v_cvt_f32_f16_sdwa v5, v31 dst_sel:DWORD dst_unused:UNUSED_PAD src0_sel:WORD_1
	v_cvt_f32_f16_e32 v6, v32
	v_cvt_f32_f16_sdwa v7, v32 dst_sel:DWORD dst_unused:UNUSED_PAD src0_sel:WORD_1
	v_cvt_f32_f16_e32 v8, v33
	v_cvt_f32_f16_sdwa v9, v33 dst_sel:DWORD dst_unused:UNUSED_PAD src0_sel:WORD_1
	s_mov_b64 vcc, s[14:15]
	v_mul_f32_e32 v2, v34, v2
	v_mul_f32_e32 v3, v34, v3
	v_mul_f32_e32 v4, v34, v4
	v_mul_f32_e32 v5, v34, v5
	v_mul_f32_e32 v6, v34, v6
	v_mul_f32_e32 v7, v34, v7
	v_mul_f32_e32 v8, v34, v8
	v_mul_f32_e32 v9, v34, v9
	v_cndmask_b32_e32 v2, 0, v2, vcc
	v_cndmask_b32_e32 v3, 0, v3, vcc
	v_cndmask_b32_e32 v4, 0, v4, vcc
	v_cndmask_b32_e32 v5, 0, v5, vcc
	v_cndmask_b32_e32 v6, 0, v6, vcc
	v_cndmask_b32_e32 v7, 0, v7, vcc
	v_cndmask_b32_e32 v8, 0, v8, vcc
	v_cndmask_b32_e32 v9, 0, v9, vcc
	v_pk_add_f32 v[42:43], v[42:43], v[2:3]
	v_pk_add_f32 v[40:41], v[40:41], v[4:5]
	v_pk_add_f32 v[38:39], v[38:39], v[6:7]
	v_pk_add_f32 v[36:37], v[36:37], v[8:9]
	s_movk_i32 s0, 0x110
	v_cvt_pk_f16_f32 v5, v36, v37
	v_cvt_pk_f16_f32 v4, v38, v39
	v_cvt_pk_f16_f32 v3, v40, v41
	v_cvt_pk_f16_f32 v2, v42, v43
	v_and_b32_e32 v46, 30, v35
	v_mad_u32_u24 v46, v46, s0, v26
	ds_write_b128 v46, v[2:5]
	v_or_b32_e32 v62, 1, v35
	v_mov_b32_e32 v46, 0x3200
	v_lshl_add_u32 v46, v62, 2, v46
	ds_read2_b32 v[44:45], v46 offset1:1
	v_add_u32_e32 v47, s24, v62
	s_mov_b32 s0, 0x186a0
	v_cmp_gt_i32_e32 vcc, s0, v47
	s_mov_b64 s[14:15], vcc
	v_min_i32_e32 v47, 0x1869f, v47
	v_lshl_add_u32 v47, v47, 8, v26
	global_load_dwordx4 v[30:33], v47, s[4:5]
	v_mov_b32_e32 v36, 0
	v_mov_b32_e32 v37, 0
	v_mov_b32_e32 v38, 0
	v_mov_b32_e32 v39, 0
	v_mov_b32_e32 v40, 0
	v_mov_b32_e32 v41, 0
	v_mov_b32_e32 v42, 0
	v_mov_b32_e32 v43, 0
	s_waitcnt lgkmcnt(0)
	v_lshl_add_u32 v29, v44, 8, v26
	v_cmp_lt_i32_e64 s[16:17], v44, v45
	v_add_u32_e32 v46, 1, v44
	v_cmp_lt_i32_e64 s[18:19], v46, v45
	v_add_u32_e32 v46, 2, v44
	v_cmp_lt_i32_e64 s[20:21], v46, v45
	v_add_u32_e32 v46, 3, v44
	v_cmp_lt_i32_e64 s[22:23], v46, v45
	v_sub_u32_e32 v27, v44, v28
	v_lshl_add_u32 v27, v27, 2, s1
	s_mov_b64 exec, s[16:17]
	ds_read_b32 v10, v27 offset:0
	s_mov_b64 exec, s[18:19]
	ds_read_b32 v11, v27 offset:4
	s_mov_b64 exec, s[20:21]
	ds_read_b32 v12, v27 offset:8
	s_mov_b64 exec, s[22:23]
	ds_read_b32 v13, v27 offset:12
	s_mov_b64 exec, s[16:17]
	global_load_dwordx4 v[2:5], v29, s[30:31] offset:0
	s_waitcnt lgkmcnt(0)
	v_lshl_add_u32 v10, v10, 8, v26
	global_load_dwordx4 v[6:9], v10, s[4:5]
	ds_read_b32 v10, v27 offset:16
	s_mov_b64 exec, s[18:19]
	global_load_dwordx4 v[14:17], v29, s[30:31] offset:256
	s_waitcnt lgkmcnt(0)
	v_lshl_add_u32 v11, v11, 8, v26
	global_load_dwordx4 v[18:21], v11, s[4:5]
	ds_read_b32 v11, v27 offset:20
	s_mov_b64 exec, s[20:21]
	global_load_dwordx4 v[22:25], v29, s[30:31] offset:512
	s_waitcnt lgkmcnt(0)
	v_lshl_add_u32 v12, v12, 8, v26
	global_load_dwordx4 v[50:53], v12, s[4:5]
	ds_read_b32 v12, v27 offset:24
	s_mov_b64 exec, s[22:23]
	global_load_dwordx4 v[54:57], v29, s[30:31] offset:768
	s_waitcnt lgkmcnt(0)
	v_lshl_add_u32 v13, v13, 8, v26
	global_load_dwordx4 v[58:61], v13, s[4:5]
	ds_read_b32 v13, v27 offset:28
	s_mov_b64 exec, s[2:3]
	s_cmp_eq_u64 s[16:17], 0
	s_cbranch_scc1 .Ll1e_p2_empty
	s_mov_b64 exec, s[16:17]
	s_waitcnt vmcnt(6)
	v_fma_mix_f32 v46, v6, 1.0, v2 op_sel_hi:[1,0,1]
	v_fma_mix_f32 v47, v6, 1.0, v2 op_sel:[1,0,1] op_sel_hi:[1,0,1]
	v_fma_mix_f32 v48, v7, 1.0, v3 op_sel_hi:[1,0,1]
	v_fma_mix_f32 v49, v7, 1.0, v3 op_sel:[1,0,1] op_sel_hi:[1,0,1]
	v_max_f32_e32 v46, 0, v46
	v_max_f32_e32 v47, 0, v47
	v_max_f32_e32 v48, 0, v48
	v_max_f32_e32 v49, 0, v49
	v_pk_add_f32 v[42:43], v[42:43], v[46:47]
	v_pk_add_f32 v[40:41], v[40:41], v[48:49]
	v_fma_mix_f32 v46, v8, 1.0, v4 op_sel_hi:[1,0,1]
	v_fma_mix_f32 v47, v8, 1.0, v4 op_sel:[1,0,1] op_sel_hi:[1,0,1]
	v_fma_mix_f32 v48, v9, 1.0, v5 op_sel_hi:[1,0,1]
	v_fma_mix_f32 v49, v9, 1.0, v5 op_sel:[1,0,1] op_sel_hi:[1,0,1]
	v_max_f32_e32 v46, 0, v46
	v_max_f32_e32 v47, 0, v47
	v_max_f32_e32 v48, 0, v48
	v_max_f32_e32 v49, 0, v49
	v_pk_add_f32 v[38:39], v[38:39], v[46:47]
	v_pk_add_f32 v[36:37], v[36:37], v[48:49]
	v_add_u32_e32 v46, 4, v44
	v_cmp_lt_i32_e64 s[16:17], v46, v45
	s_mov_b64 exec, s[16:17]
	global_load_dwordx4 v[2:5], v29, s[30:31] offset:1024
	s_waitcnt lgkmcnt(0)
	v_lshl_add_u32 v10, v10, 8, v26
	global_load_dwordx4 v[6:9], v10, s[4:5]
	ds_read_b32 v10, v27 offset:32
	s_mov_b64 exec, s[18:19]
	s_waitcnt vmcnt(6)
	v_fma_mix_f32 v46, v18, 1.0, v14 op_sel_hi:[1,0,1]
	v_fma_mix_f32 v47, v18, 1.0, v14 op_sel:[1,0,1] op_sel_hi:[1,0,1]
	v_fma_mix_f32 v48, v19, 1.0, v15 op_sel_hi:[1,0,1]
	v_fma_mix_f32 v49, v19, 1.0, v15 op_sel:[1,0,1] op_sel_hi:[1,0,1]
	v_max_f32_e32 v46, 0, v46
	v_max_f32_e32 v47, 0, v47
	v_max_f32_e32 v48, 0, v48
	v_max_f32_e32 v49, 0, v49
	v_pk_add_f32 v[42:43], v[42:43], v[46:47]
	v_pk_add_f32 v[40:41], v[40:41], v[48:49]
	v_fma_mix_f32 v46, v20, 1.0, v16 op_sel_hi:[1,0,1]
	v_fma_mix_f32 v47, v20, 1.0, v16 op_sel:[1,0,1] op_sel_hi:[1,0,1]
	v_fma_mix_f32 v48, v21, 1.0, v17 op_sel_hi:[1,0,1]
	v_fma_mix_f32 v49, v21, 1.0, v17 op_sel:[1,0,1] op_sel_hi:[1,0,1]
	v_max_f32_e32 v46, 0, v46
	v_max_f32_e32 v47, 0, v47
	v_max_f32_e32 v48, 0, v48
	v_max_f32_e32 v49, 0, v49
	v_pk_add_f32 v[38:39], v[38:39], v[46:47]
	v_pk_add_f32 v[36:37], v[36:37], v[48:49]
	v_add_u32_e32 v46, 5, v44
	v_cmp_lt_i32_e64 s[18:19], v46, v45
	s_mov_b64 exec, s[18:19]
	global_load_dwordx4 v[14:17], v29, s[30:31] offset:1280
	s_waitcnt lgkmcnt(0)
	v_lshl_add_u32 v11, v11, 8, v26
	global_load_dwordx4 v[18:21], v11, s[4:5]
	ds_read_b32 v11, v27 offset:36
	s_mov_b64 exec, s[20:21]
	s_waitcnt vmcnt(6)
	v_fma_mix_f32 v46, v50, 1.0, v22 op_sel_hi:[1,0,1]
	v_fma_mix_f32 v47, v50, 1.0, v22 op_sel:[1,0,1] op_sel_hi:[1,0,1]
	v_fma_mix_f32 v48, v51, 1.0, v23 op_sel_hi:[1,0,1]
	v_fma_mix_f32 v49, v51, 1.0, v23 op_sel:[1,0,1] op_sel_hi:[1,0,1]
	v_max_f32_e32 v46, 0, v46
	v_max_f32_e32 v47, 0, v47
	v_max_f32_e32 v48, 0, v48
	v_max_f32_e32 v49, 0, v49
	v_pk_add_f32 v[42:43], v[42:43], v[46:47]
	v_pk_add_f32 v[40:41], v[40:41], v[48:49]
	v_fma_mix_f32 v46, v52, 1.0, v24 op_sel_hi:[1,0,1]
	v_fma_mix_f32 v47, v52, 1.0, v24 op_sel:[1,0,1] op_sel_hi:[1,0,1]
	v_fma_mix_f32 v48, v53, 1.0, v25 op_sel_hi:[1,0,1]
	v_fma_mix_f32 v49, v53, 1.0, v25 op_sel:[1,0,1] op_sel_hi:[1,0,1]
	v_max_f32_e32 v46, 0, v46
	v_max_f32_e32 v47, 0, v47
	v_max_f32_e32 v48, 0, v48
	v_max_f32_e32 v49, 0, v49
	v_pk_add_f32 v[38:39], v[38:39], v[46:47]
	v_pk_add_f32 v[36:37], v[36:37], v[48:49]
	v_add_u32_e32 v46, 6, v44
	v_cmp_lt_i32_e64 s[20:21], v46, v45
	s_mov_b64 exec, s[20:21]
	global_load_dwordx4 v[22:25], v29, s[30:31] offset:1536
	s_waitcnt lgkmcnt(0)
	v_lshl_add_u32 v12, v12, 8, v26
	global_load_dwordx4 v[50:53], v12, s[4:5]
	ds_read_b32 v12, v27 offset:40
	s_mov_b64 exec, s[22:23]
	s_waitcnt vmcnt(6)
	v_fma_mix_f32 v46, v58, 1.0, v54 op_sel_hi:[1,0,1]
	v_fma_mix_f32 v47, v58, 1.0, v54 op_sel:[1,0,1] op_sel_hi:[1,0,1]
	v_fma_mix_f32 v48, v59, 1.0, v55 op_sel_hi:[1,0,1]
	v_fma_mix_f32 v49, v59, 1.0, v55 op_sel:[1,0,1] op_sel_hi:[1,0,1]
	v_max_f32_e32 v46, 0, v46
	v_max_f32_e32 v47, 0, v47
	v_max_f32_e32 v48, 0, v48
	v_max_f32_e32 v49, 0, v49
	v_pk_add_f32 v[42:43], v[42:43], v[46:47]
	v_pk_add_f32 v[40:41], v[40:41], v[48:49]
	v_fma_mix_f32 v46, v60, 1.0, v56 op_sel_hi:[1,0,1]
	v_fma_mix_f32 v47, v60, 1.0, v56 op_sel:[1,0,1] op_sel_hi:[1,0,1]
	v_fma_mix_f32 v48, v61, 1.0, v57 op_sel_hi:[1,0,1]
	v_fma_mix_f32 v49, v61, 1.0, v57 op_sel:[1,0,1] op_sel_hi:[1,0,1]
	v_max_f32_e32 v46, 0, v46
	v_max_f32_e32 v47, 0, v47
	v_max_f32_e32 v48, 0, v48
	v_max_f32_e32 v49, 0, v49
	v_pk_add_f32 v[38:39], v[38:39], v[46:47]
	v_pk_add_f32 v[36:37], v[36:37], v[48:49]
	v_add_u32_e32 v46, 7, v44
	v_cmp_lt_i32_e64 s[22:23], v46, v45
	s_mov_b64 exec, s[22:23]
	global_load_dwordx4 v[54:57], v29, s[30:31] offset:1792
	s_waitcnt lgkmcnt(0)
	v_lshl_add_u32 v13, v13, 8, v26
	global_load_dwordx4 v[58:61], v13, s[4:5]
	ds_read_b32 v13, v27 offset:44
	s_mov_b64 exec, s[2:3]
	v_add_u32_e32 v44, 4, v44
	v_add_u32_e32 v27, 16, v27
	v_add_u32_e32 v29, 0x400, v29
	s_cmp_lg_u64 s[16:17], 0
	s_cbranch_scc0 .Ll1e_p2_done

.Ll1e_p2_done:
	v_cvt_f32_f16_e32 v2, v30
	v_cvt_f32_f16_sdwa v3, v30 dst_sel:DWORD dst_unused:UNUSED_PAD src0_sel:WORD_1
	v_cvt_f32_f16_e32 v4, v31
	v_cvt_f32_f16_sdwa v5, v31 dst_sel:DWORD dst_unused:UNUSED_PAD src0_sel:WORD_1
	v_cvt_f32_f16_e32 v6, v32
	v_cvt_f32_f16_sdwa v7, v32 dst_sel:DWORD dst_unused:UNUSED_PAD src0_sel:WORD_1
	v_cvt_f32_f16_e32 v8, v33
	v_cvt_f32_f16_sdwa v9, v33 dst_sel:DWORD dst_unused:UNUSED_PAD src0_sel:WORD_1
	s_mov_b64 vcc, s[14:15]
	v_mul_f32_e32 v2, v34, v2
	v_mul_f32_e32 v3, v34, v3
	v_mul_f32_e32 v4, v34, v4
	v_mul_f32_e32 v5, v34, v5
	v_mul_f32_e32 v6, v34, v6
	v_mul_f32_e32 v7, v34, v7
	v_mul_f32_e32 v8, v34, v8
	v_mul_f32_e32 v9, v34, v9
	v_cndmask_b32_e32 v2, 0, v2, vcc
	v_cndmask_b32_e32 v3, 0, v3, vcc
	v_cndmask_b32_e32 v4, 0, v4, vcc
	v_cndmask_b32_e32 v5, 0, v5, vcc
	v_cndmask_b32_e32 v6, 0, v6, vcc
	v_cndmask_b32_e32 v7, 0, v7, vcc
	v_cndmask_b32_e32 v8, 0, v8, vcc
	v_cndmask_b32_e32 v9, 0, v9, vcc
	v_pk_add_f32 v[42:43], v[42:43], v[2:3]
	v_pk_add_f32 v[40:41], v[40:41], v[4:5]
	v_pk_add_f32 v[38:39], v[38:39], v[6:7]
	v_pk_add_f32 v[36:37], v[36:37], v[8:9]
	v_mov_b32_e32 v27, v62
	v_mov_b32_e32 v34, v42
	v_mov_b32_e32 v35, v43
	v_mov_b32_e32 v46, v40
	v_mov_b32_e32 v47, v41
	v_mov_b32_e32 v48, v38
	v_mov_b32_e32 v49, v39
	v_mov_b32_e32 v50, v36
	v_mov_b32_e32 v51, v37
	s_branch .LBB5_61

	.amdhsa_kernel _Z12layer_kernelILb0ELi256ELi32EEvPKDv8_DF16_PKfPS0_PiS6_S6_S2_S4_S5_PfPK15HIP_vector_typeIiLj2EEPKi
		.amdhsa_group_segment_fixed_size 12932
		.amdhsa_private_segment_fixed_size 0
		.amdhsa_kernarg_size 352
		.amdhsa_user_sgpr_count 2
		.amdhsa_user_sgpr_dispatch_ptr 0
		.amdhsa_user_sgpr_queue_ptr 0
		.amdhsa_user_sgpr_kernarg_segment_ptr 1
		.amdhsa_user_sgpr_dispatch_id 0
		.amdhsa_user_sgpr_kernarg_preload_length 0
		.amdhsa_user_sgpr_kernarg_preload_offset 0
		.amdhsa_user_sgpr_private_segment_size 0
		.amdhsa_uses_dynamic_stack 0
		.amdhsa_enable_private_segment 0
		.amdhsa_system_sgpr_workgroup_id_x 1
		.amdhsa_system_sgpr_workgroup_id_y 0
		.amdhsa_system_sgpr_workgroup_id_z 0
		.amdhsa_system_sgpr_workgroup_info 0
		.amdhsa_system_vgpr_workitem_id 0
		.amdhsa_next_free_vgpr 64
		.amdhsa_next_free_sgpr 32
		.amdhsa_accum_offset 64
		.amdhsa_reserve_vcc 1
		.amdhsa_float_round_mode_32 0
		.amdhsa_float_round_mode_16_64 0
		.amdhsa_float_denorm_mode_32 3
		.amdhsa_float_denorm_mode_16_64 3
		.amdhsa_dx10_clamp 1
		.amdhsa_ieee_mode 1
		.amdhsa_fp16_overflow 0
		.amdhsa_tg_split 0
		.amdhsa_exception_fp_ieee_invalid_op 0
		.amdhsa_exception_fp_denorm_src 0
		.amdhsa_exception_fp_ieee_div_zero 0
		.amdhsa_exception_fp_ieee_overflow 0
		.amdhsa_exception_fp_ieee_underflow 0
		.amdhsa_exception_fp_ieee_inexact 0
		.amdhsa_exception_int_div_zero 0
	.end_amdhsa_kernel

amdhsa.kernels:
  - .agpr_count:     0
    .args:
      - .actual_access:  read_only
        .address_space:  global
        .offset:         0
        .size:           8
        .value_kind:     global_buffer
      - .address_space:  global
        .offset:         8
        .size:           8
        .value_kind:     global_buffer
      - .actual_access:  read_only
        .address_space:  global
        .offset:         16
        .size:           8
        .value_kind:     global_buffer
      - .actual_access:  read_only
        .address_space:  global
        .offset:         24
        .size:           8
        .value_kind:     global_buffer
      - .actual_access:  write_only
        .address_space:  global
        .offset:         32
        .size:           8
        .value_kind:     global_buffer
      - .actual_access:  read_only
        .address_space:  global
        .offset:         40
        .size:           8
        .value_kind:     global_buffer
      - .actual_access:  write_only
        .address_space:  global
        .offset:         48
        .size:           8
        .value_kind:     global_buffer
      - .actual_access:  write_only
        .address_space:  global
        .offset:         56
        .size:           8
        .value_kind:     global_buffer
    .group_segment_fixed_size: 6400
    .kernarg_segment_align: 8
    .kernarg_segment_size: 64
    .language:       OpenCL C
    .language_version:
      - 2
      - 0
    .max_flat_workgroup_size: 1024
    .name:           _Z17prep_count_kernelPKfPDv8_DF16_S0_S0_S2_PKiPiP15HIP_vector_typeIfLj4EE
    .private_segment_fixed_size: 0
    .sgpr_count:     22
    .sgpr_spill_count: 0
    .symbol:         _Z17prep_count_kernelPKfPDv8_DF16_S0_S0_S2_PKiPiP15HIP_vector_typeIfLj4EE.kd
    .uniform_work_group_size: 1
    .uses_dynamic_stack: false
    .vgpr_count:     22
    .vgpr_spill_count: 0
    .wavefront_size: 64
  - .agpr_count:     0
    .args:
      - .actual_access:  read_only
        .address_space:  global
        .offset:         0
        .size:           8
        .value_kind:     global_buffer
      - .actual_access:  read_only
        .address_space:  global
        .offset:         8
        .size:           8
        .value_kind:     global_buffer
      - .actual_access:  read_only
        .address_space:  global
        .offset:         16
        .size:           8
        .value_kind:     global_buffer
      - .actual_access:  write_only
        .address_space:  global
        .offset:         24
        .size:           8
        .value_kind:     global_buffer
      - .actual_access:  write_only
        .address_space:  global
        .offset:         32
        .size:           8
        .value_kind:     global_buffer
    .group_segment_fixed_size: 124704
    .kernarg_segment_align: 8
    .kernarg_segment_size: 40
    .language:       OpenCL C
    .language_version:
      - 2
      - 0
    .max_flat_workgroup_size: 1024
    .name:           _Z14scatter_kernelPKiS0_S0_PiP15HIP_vector_typeIiLj2EE
    .private_segment_fixed_size: 0
    .sgpr_count:     55
    .sgpr_spill_count: 0
    .symbol:         _Z14scatter_kernelPKiS0_S0_PiP15HIP_vector_typeIiLj2EE.kd
    .uniform_work_group_size: 1
    .uses_dynamic_stack: false
    .vgpr_count:     128
    .vgpr_spill_count: 0
    .wavefront_size: 64
  - .agpr_count:     0
    .args:
      - .actual_access:  read_only
        .address_space:  global
        .offset:         0
        .size:           8
        .value_kind:     global_buffer
      - .address_space:  global
        .offset:         8
        .size:           8
        .value_kind:     global_buffer
      - .address_space:  global
        .offset:         16
        .size:           8
        .value_kind:     global_buffer
      - .actual_access:  read_only
        .address_space:  global
        .offset:         24
        .size:           8
        .value_kind:     global_buffer
      - .actual_access:  read_only
        .address_space:  global
        .offset:         32
        .size:           8
        .value_kind:     global_buffer
      - .actual_access:  read_only
        .address_space:  global
        .offset:         40
        .size:           8
        .value_kind:     global_buffer
      - .offset:         48
        .size:           4
        .value_kind:     hidden_block_count_x
      - .offset:         52
        .size:           4
        .value_kind:     hidden_block_count_y
      - .offset:         56
        .size:           4
        .value_kind:     hidden_block_count_z
      - .offset:         60
        .size:           2
        .value_kind:     hidden_group_size_x
      - .offset:         62
        .size:           2
        .value_kind:     hidden_group_size_y
      - .offset:         64
        .size:           2
        .value_kind:     hidden_group_size_z
      - .offset:         66
        .size:           2
        .value_kind:     hidden_remainder_x
      - .offset:         68
        .size:           2
        .value_kind:     hidden_remainder_y
      - .offset:         70
        .size:           2
        .value_kind:     hidden_remainder_z
      - .offset:         88
        .size:           8
        .value_kind:     hidden_global_offset_x
      - .offset:         96
        .size:           8
        .value_kind:     hidden_global_offset_y
      - .offset:         104
        .size:           8
        .value_kind:     hidden_global_offset_z
      - .offset:         112
        .size:           2
        .value_kind:     hidden_grid_dims
    .group_segment_fixed_size: 1024
    .kernarg_segment_align: 8
    .kernarg_segment_size: 304
    .language:       OpenCL C
    .language_version:
      - 2
      - 0
    .max_flat_workgroup_size: 256
    .name:           _Z9bn_kernelPKDv8_DF16_S1_PS_PKfS4_S4_
    .private_segment_fixed_size: 0
    .sgpr_count:     20
    .sgpr_spill_count: 0
    .symbol:         _Z9bn_kernelPKDv8_DF16_S1_PS_PKfS4_S4_.kd
    .uniform_work_group_size: 1
    .uses_dynamic_stack: false
    .vgpr_count:     64
    .vgpr_spill_count: 0
    .wavefront_size: 64
  - .agpr_count:     0
    .args:
      - .actual_access:  read_only
        .address_space:  global
        .offset:         0
        .size:           8
        .value_kind:     global_buffer
      - .actual_access:  read_only
        .address_space:  global
        .offset:         8
        .size:           8
        .value_kind:     global_buffer
      - .actual_access:  read_only
        .address_space:  global
        .offset:         16
        .size:           8
        .value_kind:     global_buffer
      - .actual_access:  read_only
        .address_space:  global
        .offset:         24
        .size:           8
        .value_kind:     global_buffer
      - .actual_access:  read_only
        .address_space:  global
        .offset:         32
        .size:           8
        .value_kind:     global_buffer
      - .actual_access:  read_only
        .address_space:  global
        .offset:         40
        .size:           8
        .value_kind:     global_buffer
      - .actual_access:  read_only
        .address_space:  global
        .offset:         48
        .size:           8
        .value_kind:     global_buffer
      - .actual_access:  write_only
        .address_space:  global
        .offset:         56
        .size:           8
        .value_kind:     global_buffer
      - .offset:         64
        .size:           4
        .value_kind:     hidden_block_count_x
      - .offset:         68
        .size:           4
        .value_kind:     hidden_block_count_y
      - .offset:         72
        .size:           4
        .value_kind:     hidden_block_count_z
      - .offset:         76
        .size:           2
        .value_kind:     hidden_group_size_x
      - .offset:         78
        .size:           2
        .value_kind:     hidden_group_size_y
      - .offset:         80
        .size:           2
        .value_kind:     hidden_group_size_z
      - .offset:         82
        .size:           2
        .value_kind:     hidden_remainder_x
      - .offset:         84
        .size:           2
        .value_kind:     hidden_remainder_y
      - .offset:         86
        .size:           2
        .value_kind:     hidden_remainder_z
      - .offset:         104
        .size:           8
        .value_kind:     hidden_global_offset_x
      - .offset:         112
        .size:           8
        .value_kind:     hidden_global_offset_y
      - .offset:         120
        .size:           8
        .value_kind:     hidden_global_offset_z
      - .offset:         128
        .size:           2
        .value_kind:     hidden_grid_dims
    .group_segment_fixed_size: 34816
    .kernarg_segment_align: 8
    .kernarg_segment_size: 320
    .language:       OpenCL C
    .language_version:
      - 2
      - 0
    .max_flat_workgroup_size: 512
    .name:           _Z12final_kernelPKDv8_DF16_S1_PKfS3_S3_S1_S3_Pf
    .private_segment_fixed_size: 0
    .sgpr_count:     34
    .sgpr_spill_count: 0
    .symbol:         _Z12final_kernelPKDv8_DF16_S1_PKfS3_S3_S1_S3_Pf.kd
    .uniform_work_group_size: 1
    .uses_dynamic_stack: false
    .vgpr_count:     60
    .vgpr_spill_count: 0
    .wavefront_size: 64
  - .agpr_count:     0
    .args:
      - .actual_access:  read_only
        .address_space:  global
        .offset:         0
        .size:           8
        .value_kind:     global_buffer
      - .actual_access:  read_only
        .address_space:  global
        .offset:         8
        .size:           8
        .value_kind:     global_buffer
      - .address_space:  global
        .offset:         16
        .size:           8
        .value_kind:     global_buffer
      - .actual_access:  write_only
        .address_space:  global
        .offset:         24
        .size:           8
        .value_kind:     global_buffer
      - .address_space:  global
        .offset:         32
        .size:           8
        .value_kind:     global_buffer
      - .address_space:  global
        .offset:         40
        .size:           8
        .value_kind:     global_buffer
      - .actual_access:  read_only
        .address_space:  global
        .offset:         48
        .size:           8
        .value_kind:     global_buffer
      - .actual_access:  read_only
        .address_space:  global
        .offset:         56
        .size:           8
        .value_kind:     global_buffer
      - .address_space:  global
        .offset:         64
        .size:           8
        .value_kind:     global_buffer
      - .address_space:  global
        .offset:         72
        .size:           8
        .value_kind:     global_buffer
      - .actual_access:  read_only
        .address_space:  global
        .offset:         80
        .size:           8
        .value_kind:     global_buffer
      - .actual_access:  read_only
        .address_space:  global
        .offset:         88
        .size:           8
        .value_kind:     global_buffer
      - .offset:         96
        .size:           4
        .value_kind:     hidden_block_count_x
      - .offset:         100
        .size:           4
        .value_kind:     hidden_block_count_y
      - .offset:         104
        .size:           4
        .value_kind:     hidden_block_count_z
      - .offset:         108
        .size:           2
        .value_kind:     hidden_group_size_x
      - .offset:         110
        .size:           2
        .value_kind:     hidden_group_size_y
      - .offset:         112
        .size:           2
        .value_kind:     hidden_group_size_z
      - .offset:         114
        .size:           2
        .value_kind:     hidden_remainder_x
      - .offset:         116
        .size:           2
        .value_kind:     hidden_remainder_y
      - .offset:         118
        .size:           2
        .value_kind:     hidden_remainder_z
      - .offset:         136
        .size:           8
        .value_kind:     hidden_global_offset_x
      - .offset:         144
        .size:           8
        .value_kind:     hidden_global_offset_y
      - .offset:         152
        .size:           8
        .value_kind:     hidden_global_offset_z
      - .offset:         160
        .size:           2
        .value_kind:     hidden_grid_dims
    .group_segment_fixed_size: 26384
    .kernarg_segment_align: 8
    .kernarg_segment_size: 352
    .language:       OpenCL C
    .language_version:
      - 2
      - 0
    .max_flat_workgroup_size: 512
    .name:           _Z12layer_kernelILb1ELi512ELi64EEvPKDv8_DF16_PKfPS0_PiS6_S6_S2_S4_S5_PfPK15HIP_vector_typeIiLj2EEPKi
    .private_segment_fixed_size: 0
    .sgpr_count:     52
    .sgpr_spill_count: 0
    .symbol:         _Z12layer_kernelILb1ELi512ELi64EEvPKDv8_DF16_PKfPS0_PiS6_S6_S2_S4_S5_PfPK15HIP_vector_typeIiLj2EEPKi.kd
    .uniform_work_group_size: 1
    .uses_dynamic_stack: false
    .vgpr_count:     61
    .vgpr_spill_count: 0
    .wavefront_size: 64
  - .agpr_count:     0
    .args:
      - .actual_access:  read_only
        .address_space:  global
        .offset:         0
        .size:           8
        .value_kind:     global_buffer
      - .actual_access:  read_only
        .address_space:  global
        .offset:         8
        .size:           8
        .value_kind:     global_buffer
      - .actual_access:  read_only
        .address_space:  global
        .offset:         16
        .size:           8
        .value_kind:     global_buffer
      - .actual_access:  read_only
        .address_space:  global
        .offset:         24
        .size:           8
        .value_kind:     global_buffer
      - .actual_access:  read_only
        .address_space:  global
        .offset:         32
        .size:           8
        .value_kind:     global_buffer
      - .actual_access:  read_only
        .address_space:  global
        .offset:         40
        .size:           8
        .value_kind:     global_buffer
      - .actual_access:  read_only
        .address_space:  global
        .offset:         48
        .size:           8
        .value_kind:     global_buffer
      - .actual_access:  read_only
        .address_space:  global
        .offset:         56
        .size:           8
        .value_kind:     global_buffer
      - .address_space:  global
        .offset:         64
        .size:           8
        .value_kind:     global_buffer
      - .address_space:  global
        .offset:         72
        .size:           8
        .value_kind:     global_buffer
      - .actual_access:  read_only
        .address_space:  global
        .offset:         80
        .size:           8
        .value_kind:     global_buffer
      - .actual_access:  read_only
        .address_space:  global
        .offset:         88
        .size:           8
        .value_kind:     global_buffer
      - .offset:         96
        .size:           4
        .value_kind:     hidden_block_count_x
      - .offset:         100
        .size:           4
        .value_kind:     hidden_block_count_y
      - .offset:         104
        .size:           4
        .value_kind:     hidden_block_count_z
      - .offset:         108
        .size:           2
        .value_kind:     hidden_group_size_x
      - .offset:         110
        .size:           2
        .value_kind:     hidden_group_size_y
      - .offset:         112
        .size:           2
        .value_kind:     hidden_group_size_z
      - .offset:         114
        .size:           2
        .value_kind:     hidden_remainder_x
      - .offset:         116
        .size:           2
        .value_kind:     hidden_remainder_y
      - .offset:         118
        .size:           2
        .value_kind:     hidden_remainder_z
      - .offset:         136
        .size:           8
        .value_kind:     hidden_global_offset_x
      - .offset:         144
        .size:           8
        .value_kind:     hidden_global_offset_y
      - .offset:         152
        .size:           8
        .value_kind:     hidden_global_offset_z
      - .offset:         160
        .size:           2
        .value_kind:     hidden_grid_dims
    .group_segment_fixed_size: 12932
    .kernarg_segment_align: 8
    .kernarg_segment_size: 352
    .language:       OpenCL C
    .language_version:
      - 2
      - 0
    .max_flat_workgroup_size: 256
    .name:           _Z12layer_kernelILb0ELi256ELi32EEvPKDv8_DF16_PKfPS0_PiS6_S6_S2_S4_S5_PfPK15HIP_vector_typeIiLj2EEPKi
    .private_segment_fixed_size: 0
    .sgpr_count:     38
    .sgpr_spill_count: 0
    .symbol:         _Z12layer_kernelILb0ELi256ELi32EEvPKDv8_DF16_PKfPS0_PiS6_S6_S2_S4_S5_PfPK15HIP_vector_typeIiLj2EEPKi.kd
    .uniform_work_group_size: 1
    .uses_dynamic_stack: false
    .vgpr_count:     64
    .vgpr_spill_count: 0
    .wavefront_size: 64
